# HGRN chunk chain embedded in the first full-head attention unit (one chain step per KV tile, loads one tile ahead) instead of a serial pre-pass
# baseline (speedup 1.0000x reference)
; #define LAS __attribute__((address_space(3)))
; #define H2_LOAD(V, D, C0) do { _Pragma("unroll") for (int u = 0; u < 6; ++u) { V[u] = __builtin_nontemporal_load(kv + (size_t)((C0) + u) * 8 * 16384); D[u] = dc[(size_t)((C0) + u) * 8 * 128]; } } while (0)
; #define H2_STEP(V, D, C0) do { _Pragma("unroll") for (int u = 0; u < 6; ++u) { sb[(size_t)((C0) + u) * 8 * 16384] = f2bf(S); S = fmaf(D[u], S, V[u]); } } while (0)
; __device__ __forceinline__ void ph_hgrn_chain2(const P& p, int gt, int nt) {
;   for (int idx = gt; idx < 8 * 128 * 128; idx += nt) {
;     const int hd = idx >> 14, ed = idx & 16383, d = ed & 127;
;     const float* kv = WSP(float, WS_KVC) + (size_t)hd * 16384 + ed; const float* dc = WSP(float, WS_DEC) + hd * 128 + d; bf16_t* sb = WSP(bf16_t, WS_SB) + (size_t)hd * 16384 + ed;
;     float S = 0.f;
;     float a[6], da[6], b2[6], db[6];
;     ...
;     H2_LOAD(a, da, 0);
; #pragma unroll 1
;     for (int c0 = 0; c0 < HG_NCH; c0 += 12) {
;       H2_LOAD(b2, db, c0 + 6); H2_STEP(a, da, c0);
;       if (c0 + 12 < HG_NCH) H2_LOAD(a, da, c0 + 12);
;       H2_STEP(b2, db, c0 + 6);
;     }
; __global__ void __launch_bounds__(NTHR, 2) mega(MArgs a) {
;     ...
;     if (IN(b + 3)) { LDP();
;       if (l == 0 && G > 16) { if ((int)blockIdx.x >= 8) ph_hgrn_chain2(p, gt - 8 * NTHR, nt - 8 * NTHR); }
;       else ph_hgrn_chain2(p, gt, nt);
;       for (int rep = 0; rep < REP_A; ++rep) attn::phase(p, l, l == 0, G, (int)blockIdx.x, (LAS char*)lds, ltid); }
.LBB0_393:
	s_andn2_b64 vcc, exec, s[0:1]
	s_cbranch_vccnz .LBB0_526
	v_readlane_b32 s0, v252, 0
	v_readlane_b32 s1, v252, 1
	v_mov_b32_e32 v0, v97
	s_load_dwordx2 s[12:13], s[0:1], 0x60
	s_nop 0
	s_load_dwordx2 s[0:1], s[0:1], 0xe0
	v_readlane_b32 s3, v252, 5
	v_mbcnt_lo_u32_b32 v0, -1, v0
	v_mbcnt_hi_u32_b32 v12, -1, v0
	v_readlane_b32 s2, v252, 6
	s_mov_b32 s4, s81
	v_readlane_b32 s6, v255, 18
	v_readlane_b32 s4, v253, 31
	v_readlane_b32 s3, v252, 11
	v_readlane_b32 s5, v253, 32
	v_readlane_b32 s7, v255, 19
	v_add_u32_e32 v196, s3, v12
	v_readlane_b32 s3, v254, 61
	s_and_b64 s[4:5], s[4:5], s[6:7]
	s_andn2_b64 vcc, exec, s[4:5]
	v_add_u32_e32 v13, s3, v196
	s_movk_i32 s55, 0x84
	s_cmp_lg_u32 s2, 0x20000
	s_cbranch_scc1 .Lch_old
	s_mov_b32 s55, -1
	s_branch .LBB0_413
.Lch_old:
	s_mov_b64 s[6:7], -1
	s_cbranch_vccz .LBB0_403
	s_mov_b32 s3, 0x20000
	v_cmp_gt_i32_e32 vcc, s3, v13
	s_and_saveexec_b64 s[14:15], vcc
	s_cbranch_execz .LBB0_402
	s_waitcnt lgkmcnt(0)
	s_add_u32 s18, s0, 0x33b5e000
	s_addc_u32 s19, s1, 0
	v_readlane_b32 s3, v254, 62
	s_add_u32 s20, s0, 0x37d5e000
	s_addc_u32 s21, s1, 0
	v_add_u16_e32 v14, s3, v12
	v_readlane_b32 s3, v254, 63
	s_mov_b64 s[22:23], 0
	v_mov_b32_e32 v16, v13
	v_add_u16_e32 v15, s3, v12
	s_branch .LBB0_398

; __device__ __forceinline__ int v_st(int k, int c) { const int kk = (k & ~0xC) | ((k & 4) << 1) | ((k & 8) >> 1); return ((kk >> 3) * 4 + (c >> 5)) * 512 + ((kk & 7) * 32 + (c & 31)) * 2; }
; __device__ __forceinline__ int v_rd_base(int lane) { return ((lane & 3) << 3) | (((lane >> 2) & 3) << 6) | (((lane >> 4) & 1) << 5) | (((lane >> 5) & 1) << 8); }
; #define SWRITE(b, i) do { *(LAS bf16x8*)(V_lds + (b) * SHM_V + vst0) = sr_[i].vs0;          \
;     *(LAS bf16x8*)(V_lds + (b) * SHM_V + vst1) = sr_[i].vs1; int kc = sc * 2;               \
;     *(LAS bf16x8*)(K_lds + (b) * SHM_K + KSWZ(sr, kc)) = sr_[i].ks0;                       \
;     *(LAS bf16x8*)(K_lds + (b) * SHM_K + KSWZ(32 + sr, kc)) = sr_[i].ks1; } while (0)
; #define SWAIT() asm volatile("s_waitcnt vmcnt(4)" ::: "memory")
; template <bool HALF> __device__ __forceinline__ void dense_body(const bf16_t* __restrict__ Qb, const bf16_t* __restrict__ Kh, const bf16_t* __restrict__ Vh, ...
;     ...
;   const int sr = tid >> 4, sc = (tid & 15) * 8, vst0 = v_st(sr, sc), vst1 = v_st(32 + sr, sc);
;   const int vb0 = (int)(uintptr_t)V_lds + v_rd_base(lane);
;   struct { bf16x8 vs0, vs1, ks0, ks1; } sr_[2];
;   const unsigned ko0 = (unsigned)(sr * LDKK + sc) * 2u, ko1 = ko0 + 32u * LDKK * 2u, vo0 = (unsigned)(sr * LDKV + sc) * 2u, vo1 = vo0 + 32u * LDKV * 2u;
;     ...
;   f32x16 pA0, pA1, pB0, pB1; float mnA, mnB, alA, alB; bf16x8 pa0, pa1, pa2, pa3; const int NT = seq / KVBLK;
;   const char* Kl0 = (const char*)K_lds; const char* Kl1 = (const char*)(K_lds + SHM_K);
;   constexpr int SE = 0, SO = 1;
;   SLOAD(SE, 0); asm volatile("s_waitcnt vmcnt(0)" ::: "memory"); SWRITE(0, SE); __syncthreads();
;   qkt<HALF>(pA0, pA1, Kl0, qr, r32, hi, koff); partialSM(pA0, pA1, m_reg, mnA, alA);
;   SLOAD(SO, KVBLK); if (2 < NT) SLOAD(SE, 2 * KVBLK);
;   SWAIT(); SWRITE(1, SO); __syncthreads();
; template <bool HALF> __device__ __forceinline__ void unit(const P& p, int l, int u, LAS char* lds, int tid) {
;     ...
;   const int kvh = hq < 8 ? (hq >> 2) : 2 + ((hq - 8) >> 1);
;   const bf16_t* Qb = WSP(bf16_t, WS_PROJ) + (size_t)qrow * INW + (hq < 8 ? C_AQ + hq * 128 : C_DQ + (hq - 8) * 64);
;   const bf16_t* Kh = WSP(bf16_t, WS_KALL) + kvh * 128;
;   const bf16_t* Vh = WSP(bf16_t, WS_PROJ) + (kvh < 2 ? C_AV + kvh * 128 : C_DV + (kvh - 2) * 128);
.LBB0_424:
	s_ashr_i32 s6, s2, 2
	s_add_i32 s2, s2, -8
	s_lshr_b32 s2, s2, 1
	s_add_i32 s7, s2, 2
	s_and_b64 s[2:3], s[20:21], exec
	s_cselect_b32 s3, s6, s7
	s_lshl_b32 s2, s3, 7
	s_cmp_lt_i32 s3, 2
	s_movk_i32 s3, 0x1100
	s_cselect_b32 s3, s3, 0x1500
	s_add_i32 s6, s3, s2
	s_ashr_i32 s3, s2, 31
	s_lshl_b64 s[20:21], s[2:3], 1
	s_add_u32 s34, s44, s20
	v_cvt_pk_bf16_f32 v118, v122, v36
	v_cvt_pk_bf16_f32 v119, v123, v37
	v_cvt_pk_bf16_f32 v120, v120, v28
	v_cvt_pk_bf16_f32 v121, v121, v29
	v_cvt_pk_bf16_f32 v126, v114, v32
	v_cvt_pk_bf16_f32 v127, v115, v33
	v_cvt_pk_bf16_f32 v128, v112, v24
	v_cvt_pk_bf16_f32 v129, v113, v25
	v_cvt_pk_bf16_f32 v122, v108, v26
	v_cvt_pk_bf16_f32 v123, v109, v27
	v_cvt_pk_bf16_f32 v124, v106, v20
	v_cvt_pk_bf16_f32 v125, v107, v21
	v_cvt_pk_bf16_f32 v114, v104, v22
	v_cvt_pk_bf16_f32 v115, v105, v23
	v_cvt_pk_bf16_f32 v116, v74, v16
	v_cvt_pk_bf16_f32 v117, v75, v17
	v_ashrrev_i32_e32 v16, 4, v142
	v_lshlrev_b32_e32 v17, 3, v142
	s_movk_i32 s2, 0x300
	s_addc_u32 s35, s45, s21
	s_ashr_i32 s7, s6, 31
	v_cvt_pk_bf16_f32 v110, v72, v18
	v_and_b32_e32 v18, 0x78, v17
	v_mul_lo_u32 v0, v16, s2
	s_movk_i32 s2, 0x1800
	s_lshl_b64 s[22:23], s[6:7], 1
	v_cvt_pk_bf16_f32 v111, v73, v19
	v_cvt_pk_bf16_f32 v112, v70, v12
	v_cvt_pk_bf16_f32 v113, v71, v13
	v_cvt_pk_bf16_f32 v106, v68, v14
	v_cvt_pk_bf16_f32 v107, v69, v15
	v_cvt_pk_bf16_f32 v108, v6, v8
	v_or_b32_e32 v8, v0, v18
	v_mul_lo_u32 v0, v16, s2
	s_add_u32 s38, s30, s22
	v_or_b32_e32 v0, v0, v18
	s_addc_u32 s39, s31, s23
	v_lshlrev_b32_e32 v50, 1, v0
	v_cvt_pk_bf16_f32 v109, v7, v9
	v_cvt_pk_bf16_f32 v102, v4, v10
	v_cvt_pk_bf16_f32 v103, v5, v11
	v_cvt_pk_bf16_f32 v104, v2, v64
	v_cvt_pk_bf16_f32 v105, v1, v65
	v_cvt_pk_bf16_f32 v98, v40, v46
	v_cvt_pk_bf16_f32 v99, v39, v47
	v_cvt_pk_bf16_f32 v100, v34, v42
	v_cvt_pk_bf16_f32 v101, v31, v43
	v_add_u32_e32 v48, 0x60000, v50
	v_readlane_b32 s52, v252, 4
	s_nop 3
	v_and_b32_e32 v134, 63, v142
	v_lshrrev_b32_e32 v135, 4, v134
	v_and_b32_e32 v136, 15, v134
	s_lshl_b32 s53, s52, 3
	v_add_u32_e32 v137, s53, v135
	v_xor_b32_e32 v138, v136, v135
	v_mul_u32_u24_e32 v130, 0x600, v137
	v_lshl_add_u32 v130, v138, 4, v130
	v_add_u32_e32 v139, 4, v135
	v_xor_b32_e32 v138, v136, v139
	v_add_u32_e32 v137, 4, v137
	v_mul_u32_u24_e32 v131, 0x600, v137
	v_lshl_add_u32 v131, v138, 4, v131
	v_bfe_u32 v135, v134, 2, 3
	v_add_u32_e32 v135, s53, v135
	v_and_b32_e32 v136, 4, v135
	v_and_b32_e32 v137, 8, v135
	v_and_b32_e32 v135, 0xfffffff3, v135
	v_lshl_or_b32 v135, v136, 1, v135
	v_lshrrev_b32_e32 v137, 1, v137
	v_or_b32_e32 v135, v135, v137
	v_mul_u32_u24_e32 v132, 0x3000, v135
	v_lshrrev_b32_e32 v136, 5, v134
	v_lshl_add_u32 v132, v136, 6, v132
	v_and_b32_e32 v136, 3, v134
	v_lshl_add_u32 v132, v136, 4, v132
	v_add_u32_e32 v133, 0x80, v132
	v_mov_b32_e32 v140, v132
	v_mov_b32_e32 v141, v133
	s_lshl_b32 s53, s52, 11
	s_add_i32 s52, s53, 0x8000
	s_add_i32 m0, s52, 0x0
	s_nop 0
	global_load_lds_dwordx4 v130, s[34:35]
	s_add_i32 m0, s52, 0x400
	s_nop 0
	global_load_lds_dwordx4 v131, s[34:35]
	s_add_i32 m0, s53, 0x0
	s_nop 0
	global_load_lds_dwordx4 v132, s[38:39]
	s_add_i32 m0, s53, 0x400
	s_nop 0
	global_load_lds_dwordx4 v133, s[38:39]
	s_add_u32 s48, s34, 0x18000
	s_addc_u32 s49, s35, 0
	s_add_u32 s50, s38, 0xc0000
	s_addc_u32 s51, s39, 0
	s_add_i32 m0, s52, 0x4000
	s_nop 0
	global_load_lds_dwordx4 v130, s[48:49]
	s_add_i32 m0, s52, 0x4400
	s_nop 0
	global_load_lds_dwordx4 v131, s[48:49]
	s_add_i32 m0, s53, 0x4000
	s_nop 0
	global_load_lds_dwordx4 v132, s[50:51]
	s_add_i32 m0, s53, 0x4400
	s_nop 0
	global_load_lds_dwordx4 v133, s[50:51]
	s_add_u32 s48, s48, 0x18000
	s_addc_u32 s49, s49, 0
	s_add_u32 s50, s50, 0xc0000
	s_addc_u32 s51, s51, 0
	v_lshlrev_b32_e32 v52, 1, v8
	v_add_u32_e32 v54, 0xc000, v52
	v_and_b32_e32 v20, 0xfffff0, v16
	v_lshlrev_b32_e32 v21, 1, v16
	v_lshrrev_b32_e32 v22, 1, v16
	v_and_b32_e32 v23, 3, v16
	v_add_u32_e32 v24, 32, v16
	v_and_or_b32 v20, v21, 8, v20
	v_and_or_b32 v21, v22, 4, v23
	v_and_b32_e32 v22, 0xfffff0, v24
	v_lshlrev_b32_e32 v23, 1, v24
	v_bfe_u32 v17, v17, 5, 2
	v_lshrrev_b32_e32 v20, 1, v20
	v_and_or_b32 v22, v23, 8, v22
	v_lshlrev_b32_e32 v18, 1, v18
	v_or_b32_e32 v20, v20, v17
	v_lshrrev_b32_e32 v22, 1, v22
	v_lshlrev_b32_e32 v21, 6, v21
	v_and_b32_e32 v25, 48, v18
	v_lshlrev_b32_e32 v20, 9, v20
	v_or_b32_e32 v17, v22, v17
	v_or3_b32 v20, v20, v21, v25
	v_lshlrev_b32_e32 v17, 9, v17
	v_or3_b32 v17, v17, v21, v25
	v_add_u32_e32 v205, 0, v20
	v_and_b32_e32 v19, 0x70, v142
	v_lshlrev_b32_e32 v16, 8, v16
	v_add_u32_e32 v206, 0, v17
	s_waitcnt vmcnt(0)
	v_bitop3_b32 v16, v18, v16, v19 bitop3:0xde
	v_lshlrev_b32_e32 v0, 8, v24
	v_bitop3_b32 v0, v18, v0, v19 bitop3:0xde
	v_add_u32_e32 v207, 0, v16
	v_add_u32_e32 v208, 0, v0
	v_lshlrev_b32_e32 v0, 4, v197
	v_lshlrev_b32_e32 v8, 8, v197
	v_and_b32_e32 v9, 0x70, v0
	v_bitop3_b32 v0, v96, v8, v9 bitop3:0xde
	v_add_u32_e32 v209, 0, v0
	s_waitcnt lgkmcnt(0)
	s_barrier
; __device__ __forceinline__ void partialSM(f32x16& p0, f32x16& p1, float& m_reg, float& mn, float& alpha) {
;   constexpr float C = SCALE * 1.4426950408889634f;
;   float pmax = p0[0]; for (int r = 1; r < 16; ++r) pmax = fmaxf(pmax, p0[r]); for (int r = 0; r < 16; ++r) pmax = fmaxf(pmax, p1[r]);
;   { auto rr = __builtin_amdgcn_permlane32_swap(__float_as_uint(pmax), __float_as_uint(pmax), false, false);
;     pmax = fmaxf(__uint_as_float(rr[0]), __uint_as_float(rr[1])); }
;   if (__builtin_expect(__all(pmax - m_reg <= THR / SCALE), 1)) { mn = m_reg; alpha = 1.f; }
;   else { mn = fmaxf(m_reg, pmax); alpha = __builtin_amdgcn_exp2f((m_reg - mn) * C); m_reg = mn; }
;   float mnC = -mn * C;
;   for (int r = 0; r < 16; ++r) p0[r] = fmaf(p0[r], C, mnC); for (int r = 0; r < 16; ++r) p1[r] = fmaf(p1[r], C, mnC);
;   for (int r = 0; r < 16; ++r) p0[r] = __builtin_amdgcn_exp2f(p0[r]);
; }
; __device__ __forceinline__ void finishSM(f32x16& p0, f32x16& p1, float alpha, float& l_reg, bf16x8& pa0, bf16x8& pa1, bf16x8& pa2, bf16x8& pa3) {
;   for (int r = 0; r < 16; ++r) p1[r] = __builtin_amdgcn_exp2f(p1[r]);
;   float ps = 0; for (int r = 0; r < 16; ++r) ps += p0[r]; for (int r = 0; r < 16; ++r) ps += p1[r];
;   { auto rr = __builtin_amdgcn_permlane32_swap(__float_as_uint(ps), __float_as_uint(ps), false, false);
;     ps = __uint_as_float(rr[0]) + __uint_as_float(rr[1]); }
;   l_reg = l_reg * alpha + ps;
;     ...
;   PK4(p0, 0, pa0); PK4(p0, 8, pa1); PK4(p1, 0, pa2); PK4(p1, 8, pa3);
;     ...
; }
; template <bool HALF> __device__ __forceinline__ void qkt(f32x16& p0, f32x16& p1, const char* Ks, const bf16x8* qr, int r32, int hi, int koff) {
;   p0 = f32x16{}; p1 = f32x16{};
;   for (int d0 = 0; d0 < (HALF ? 4 : 8); ++d0) { int cb = (d0 * 16 + hi * 8) * 2 + koff;
;     bf16x8 b0 = *reinterpret_cast<const bf16x8*>(Ks + KSWZ(r32, cb));
;     bf16x8 b1 = *reinterpret_cast<const bf16x8*>(Ks + KSWZ(32 + r32, cb));
;     p0 = __builtin_amdgcn_mfma_f32_32x32x16_bf16(b0, qr[d0], p0, 0, 0, 0);
;     p1 = __builtin_amdgcn_mfma_f32_32x32x16_bf16(b1, qr[d0], p1, 0, 0, 0); }
; }
	ds_read_b128 v[0:3], v209 offset:32768
	ds_read_b128 v[4:7], v209 offset:40960
	s_waitcnt lgkmcnt(1)
	v_mfma_f32_32x32x16_bf16 v[16:31], v[0:3], v[118:121], 0
	v_or_b32_e32 v0, 32, v96
	v_bitop3_b32 v0, v0, v8, v9 bitop3:0xde
	v_add_u32_e32 v221, 0, v0
	v_and_b32_e32 v76, 63, v142
	v_and_b32_e32 v10, 0x3fffffc0, v142
	s_add_i32 s46, 0, 0x10000
	v_lshl_add_u32 v200, v10, 2, s46
	s_waitcnt lgkmcnt(0)
	v_mfma_f32_32x32x16_bf16 v[32:47], v[4:7], v[118:121], 0
	ds_read_b128 v[0:3], v221 offset:32768
	ds_read_b128 v[4:7], v221 offset:40960
	v_lshlrev_b32_e32 v10, 3, v76
	s_add_u32 s6, s34, 0x18000
	s_addc_u32 s7, s35, 0
	s_add_u32 s16, s38, 0xc0000
	s_addc_u32 s17, s39, 0
	s_mov_b32 s64, s65
	s_waitcnt lgkmcnt(1)
	v_mfma_f32_32x32x16_bf16 v[16:31], v[0:3], v[126:129], v[16:31]
	v_or_b32_e32 v0, 64, v96
	v_bitop3_b32 v0, v0, v8, v9 bitop3:0xde
	v_add_u32_e32 v222, 0, v0
	s_mov_b32 s66, s65
	s_mov_b32 s67, s65
	s_mov_b32 s68, s65
	s_mov_b32 s69, s65
	s_waitcnt lgkmcnt(0)
	v_mfma_f32_32x32x16_bf16 v[32:47], v[4:7], v[126:129], v[32:47]
	ds_read_b128 v[0:3], v222 offset:32768
	ds_read_b128 v[4:7], v222 offset:40960
	s_mov_b32 s70, s65
	s_mov_b32 s71, s65
	s_mov_b32 s72, s65
	s_mov_b32 s73, s65
	s_mov_b32 s74, s65
	s_mov_b32 s75, s65
	s_waitcnt lgkmcnt(1)
	v_mfma_f32_32x32x16_bf16 v[16:31], v[0:3], v[122:125], v[16:31]
	v_or_b32_e32 v0, 0x60, v96
	v_bitop3_b32 v0, v0, v8, v9 bitop3:0xde
	v_add_u32_e32 v210, 0, v0
	s_mov_b32 s76, s65
	s_mov_b32 s77, s65
	s_mov_b32 s78, s65
	s_mov_b32 s79, s65
	s_waitcnt lgkmcnt(0)
	v_mfma_f32_32x32x16_bf16 v[32:47], v[4:7], v[122:125], v[32:47]
	ds_read_b128 v[0:3], v210 offset:32768
	ds_read_b128 v[4:7], v210 offset:40960
	v_mov_b32_e32 v51, v97
	v_mov_b32_e32 v49, v97
	v_mov_b32_e32 v53, v97
	v_mov_b32_e32 v55, v97
	v_lshl_add_u64 v[180:181], s[22:23], 0, v[50:51]
	v_lshl_add_u64 v[182:183], s[22:23], 0, v[48:49]
	s_waitcnt lgkmcnt(1)
	v_mfma_f32_32x32x16_bf16 v[16:31], v[0:3], v[114:117], v[16:31]
	v_or_b32_e32 v0, 0x80, v96
	v_bitop3_b32 v0, v0, v8, v9 bitop3:0xde
	v_add_u32_e32 v211, 0, v0
	ds_read_b128 v[0:3], v211 offset:32768
	v_lshl_add_u64 v[184:185], s[20:21], 0, v[52:53]
	v_lshl_add_u64 v[186:187], s[20:21], 0, v[54:55]
	s_mov_b32 s2, 4
	s_waitcnt lgkmcnt(1)
	v_mfma_f32_32x32x16_bf16 v[32:47], v[4:7], v[114:117], v[32:47]
	ds_read_b128 v[4:7], v211 offset:40960
	v_cmp_gt_u32_e64 s[40:41], 32, v76
	v_lshl_add_u32 v201, v197, 2, v200
	v_mov_b32_e32 v202, 0
	s_waitcnt lgkmcnt(1)
	v_mfma_f32_32x32x16_bf16 v[16:31], v[0:3], v[110:113], v[16:31]
	v_lshlrev_b32_e32 v0, 4, v76
	v_and_b32_e32 v0, 0xc0, v0
	v_and_or_b32 v11, v10, 24, v0
	v_or_b32_e32 v0, 0xa0, v96
	v_bitop3_b32 v0, v0, v8, v9 bitop3:0xde
	v_add_u32_e32 v223, 0, v0
	v_and_b32_e32 v10, 0x100, v10
	s_waitcnt lgkmcnt(0)
	v_mfma_f32_32x32x16_bf16 v[32:47], v[4:7], v[110:113], v[32:47]
	ds_read_b128 v[0:3], v223 offset:32768
	ds_read_b128 v[4:7], v223 offset:40960
	s_add_u32 s6, s34, 0x30000
	s_addc_u32 s7, s35, 0
	s_waitcnt lgkmcnt(1)
	v_mfma_f32_32x32x16_bf16 v[16:31], v[0:3], v[106:109], v[16:31]
	v_lshlrev_b32_e32 v0, 1, v76
	v_and_b32_e32 v12, 32, v0
	v_or_b32_e32 v0, 0xc0, v96
	v_bitop3_b32 v0, v0, v8, v9 bitop3:0xde
	v_add_u32_e32 v225, 0, v0
	ds_read_b128 v[0:3], v225 offset:32768
	v_or3_b32 v77, v11, v12, v10
	s_waitcnt lgkmcnt(1)
	v_mfma_f32_32x32x16_bf16 v[32:47], v[4:7], v[106:109], v[32:47]
	ds_read_b128 v[4:7], v225 offset:40960
	v_add_u32_e32 v204, 0, v77
	s_waitcnt lgkmcnt(1)
	v_mfma_f32_32x32x16_bf16 v[16:31], v[0:3], v[102:105], v[16:31]
	v_or_b32_e32 v0, 0xe0, v96
	v_bitop3_b32 v0, v0, v8, v9 bitop3:0xde
	v_add_u32_e32 v224, 0, v0
	ds_read_b128 v[0:3], v224 offset:32768
	ds_read_b128 v[72:75], v224 offset:40960
	s_add_u32 s6, s38, 0x180000
	s_addc_u32 s7, s39, 0
	s_waitcnt lgkmcnt(2)
	v_mfma_f32_32x32x16_bf16 v[32:47], v[4:7], v[102:105], v[32:47]
	s_waitcnt lgkmcnt(1)
	v_mfma_f32_32x32x16_bf16 v[16:31], v[0:3], v[98:101], v[16:31]
	v_mov_b64_e32 v[0:1], s[64:65]
	v_mov_b64_e32 v[14:15], s[78:79]
	v_mov_b64_e32 v[2:3], s[66:67]
	v_mov_b64_e32 v[4:5], s[68:69]
	v_mov_b64_e32 v[6:7], s[70:71]
	v_mov_b64_e32 v[8:9], s[72:73]
	v_mov_b64_e32 v[10:11], s[74:75]
	s_waitcnt lgkmcnt(0)
	v_mfma_f32_32x32x16_bf16 v[32:47], v[72:75], v[98:101], v[32:47]
	s_nop 2
	v_max_f32_e32 v72, v17, v17
	v_max_f32_e32 v73, v16, v16
	v_max_f32_e32 v72, v73, v72
	v_max3_f32 v72, v72, v18, v19
	v_max3_f32 v72, v72, v20, v21
	v_max3_f32 v72, v72, v22, v23
	v_max3_f32 v72, v72, v24, v25
	v_max3_f32 v72, v72, v26, v27
	v_max3_f32 v72, v72, v28, v29
	v_max3_f32 v72, v72, v30, v31
	v_max3_f32 v72, v72, v32, v33
	v_max3_f32 v72, v72, v34, v35
	v_max3_f32 v72, v72, v36, v37
	v_max3_f32 v72, v72, v38, v39
	v_max3_f32 v72, v72, v40, v41
	v_max3_f32 v72, v72, v42, v43
	v_max3_f32 v72, v72, v44, v45
	v_max3_f32 v72, v72, v46, v47
	v_mov_b32_e32 v73, v72
	s_nop 1
	v_permlane32_swap_b32_e32 v72, v73
	v_max_f32_e32 v73, v73, v73
	v_max_f32_e32 v72, v72, v72
	v_max_f32_e32 v72, v72, v73
	v_add_f32_e32 v73, 0x7149f2ca, v72
	v_cmp_ge_f32_e32 vcc, s87, v73
	s_cmp_eq_u64 vcc, exec
	v_max_f32_e32 v56, 0xf149f2ca, v72
	s_cselect_b64 vcc, -1, 0
	v_cndmask_b32_e32 v170, v56, v217, vcc
	v_sub_f32_e32 v57, 0xf149f2ca, v56
	v_mul_f32_e32 v56, 0xbe0293ee, v170
	v_fmamk_f32 v16, v16, 0x3e0293ee, v56
	v_exp_f32_e32 v163, v16
	v_fmamk_f32 v16, v17, 0x3e0293ee, v56
	v_exp_f32_e32 v177, v16
	v_fmamk_f32 v16, v18, 0x3e0293ee, v56
	v_exp_f32_e32 v164, v16
	v_fmamk_f32 v16, v19, 0x3e0293ee, v56
	v_exp_f32_e32 v188, v16
	v_fmamk_f32 v16, v20, 0x3e0293ee, v56
	v_exp_f32_e32 v176, v16
	v_fmamk_f32 v16, v21, 0x3e0293ee, v56
	v_exp_f32_e32 v189, v16
	v_fmamk_f32 v16, v22, 0x3e0293ee, v56
; #define H2_LOAD(V, D, C0) do { _Pragma("unroll") for (int u = 0; u < 6; ++u) { V[u] = __builtin_nontemporal_load(kv + (size_t)((C0) + u) * 8 * 16384); D[u] = dc[(size_t)((C0) + u) * 8 * 128]; } } while (0)
; __device__ __forceinline__ void partialSM(f32x16& p0, f32x16& p1, float& m_reg, float& mn, float& alpha) {
;   constexpr float C = SCALE * 1.4426950408889634f;
;   float pmax = p0[0]; for (int r = 1; r < 16; ++r) pmax = fmaxf(pmax, p0[r]); for (int r = 0; r < 16; ++r) pmax = fmaxf(pmax, p1[r]);
;   { auto rr = __builtin_amdgcn_permlane32_swap(__float_as_uint(pmax), __float_as_uint(pmax), false, false);
;     pmax = fmaxf(__uint_as_float(rr[0]), __uint_as_float(rr[1])); }
;   if (__builtin_expect(__all(pmax - m_reg <= THR / SCALE), 1)) { mn = m_reg; alpha = 1.f; }
;   else { mn = fmaxf(m_reg, pmax); alpha = __builtin_amdgcn_exp2f((m_reg - mn) * C); m_reg = mn; }
;   float mnC = -mn * C;
;   for (int r = 0; r < 16; ++r) p0[r] = fmaf(p0[r], C, mnC); for (int r = 0; r < 16; ++r) p1[r] = fmaf(p1[r], C, mnC);
;   for (int r = 0; r < 16; ++r) p0[r] = __builtin_amdgcn_exp2f(p0[r]);
; }
; __device__ __forceinline__ void ph_hgrn_chain2(const P& p, int gt, int nt) {
;   for (int idx = gt; idx < 8 * 128 * 128; idx += nt) {
;     const int hd = idx >> 14, ed = idx & 16383, d = ed & 127;
;     const float* kv = WSP(float, WS_KVC) + (size_t)hd * 16384 + ed; const float* dc = WSP(float, WS_DEC) + hd * 128 + d; bf16_t* sb = WSP(bf16_t, WS_SB) + (size_t)hd * 16384 + ed;
;     float S = 0.f;
;     float a[6], da[6], b2[6], db[6];
;     ...
;     H2_LOAD(a, da, 0);
	v_exp_f32_e32 v165, v16
	v_fmamk_f32 v16, v23, 0x3e0293ee, v56
	v_exp_f32_e32 v175, v16
	v_fmamk_f32 v16, v24, 0x3e0293ee, v56
	v_mul_f32_e32 v57, 0x3e0293ee, v57
	v_exp_f32_e32 v166, v16
	v_fmamk_f32 v16, v25, 0x3e0293ee, v56
	v_exp_f32_e32 v57, v57
	v_exp_f32_e32 v173, v16
	v_fmamk_f32 v16, v26, 0x3e0293ee, v56
	v_exp_f32_e32 v167, v16
	v_fmamk_f32 v16, v27, 0x3e0293ee, v56
	v_exp_f32_e32 v174, v16
	v_fmamk_f32 v16, v28, 0x3e0293ee, v56
	v_exp_f32_e32 v168, v16
	v_fmamk_f32 v16, v29, 0x3e0293ee, v56
	v_pk_fma_f32 v[146:147], v[46:47], s[10:11], v[56:57] op_sel_hi:[1,0,0]
	v_pk_fma_f32 v[152:153], v[44:45], s[10:11], v[56:57] op_sel_hi:[1,0,0]
	v_pk_fma_f32 v[156:157], v[42:43], s[10:11], v[56:57] op_sel_hi:[1,0,0]
	v_pk_fma_f32 v[148:149], v[40:41], s[10:11], v[56:57] op_sel_hi:[1,0,0]
	v_pk_fma_f32 v[150:151], v[38:39], s[10:11], v[56:57] op_sel_hi:[1,0,0]
	v_pk_fma_f32 v[154:155], v[36:37], s[10:11], v[56:57] op_sel_hi:[1,0,0]
	v_pk_fma_f32 v[158:159], v[34:35], s[10:11], v[56:57] op_sel_hi:[1,0,0]
	v_pk_fma_f32 v[160:161], v[32:33], s[10:11], v[56:57] op_sel_hi:[1,0,0]
	v_exp_f32_e32 v171, v16
	v_fmamk_f32 v16, v30, 0x3e0293ee, v56
	v_fmac_f32_e32 v56, 0x3e0293ee, v31
	v_exp_f32_e32 v169, v16
	v_exp_f32_e32 v172, v56
	v_mov_b64_e32 v[12:13], s[76:77]
	v_cndmask_b32_e64 v226, v57, 1.0, vcc
	s_add_i32 s34, 0, 0x4000
	v_mov_b64_e32 v[62:63], v[14:15]
	v_mov_b64_e32 v[46:47], v[14:15]
	v_mov_b64_e32 v[30:31], v[14:15]
	v_add_u32_e32 v203, s34, v77
	v_mov_b64_e32 v[60:61], v[12:13]
	v_mov_b64_e32 v[58:59], v[10:11]
	v_mov_b64_e32 v[56:57], v[8:9]
	v_mov_b64_e32 v[54:55], v[6:7]
	v_mov_b64_e32 v[52:53], v[4:5]
	v_mov_b64_e32 v[50:51], v[2:3]
	v_mov_b64_e32 v[48:49], v[0:1]
	v_mov_b64_e32 v[44:45], v[12:13]
	v_mov_b64_e32 v[42:43], v[10:11]
	v_mov_b64_e32 v[40:41], v[8:9]
	v_mov_b64_e32 v[38:39], v[6:7]
	v_mov_b64_e32 v[36:37], v[4:5]
	v_mov_b64_e32 v[34:35], v[2:3]
	v_mov_b64_e32 v[32:33], v[0:1]
	v_mov_b64_e32 v[28:29], v[12:13]
	v_mov_b64_e32 v[26:27], v[10:11]
	v_mov_b64_e32 v[24:25], v[8:9]
	v_mov_b64_e32 v[22:23], v[6:7]
	v_mov_b64_e32 v[20:21], v[4:5]
	v_mov_b64_e32 v[18:19], v[2:3]
	v_mov_b64_e32 v[16:17], v[0:1]
	s_waitcnt lgkmcnt(0)
	s_barrier
	s_add_i32 m0, s52, 0x0
	s_nop 0
	global_load_lds_dwordx4 v130, s[48:49]
	s_add_i32 m0, s52, 0x400
	s_nop 0
	global_load_lds_dwordx4 v131, s[48:49]
	s_add_u32 s48, s48, 0x18000
	s_addc_u32 s49, s49, 0
	s_mov_b32 s54, 0
	s_cmp_lg_u32 s55, -1
	s_cbranch_scc1 .Lch_noinit
	v_readlane_b32 s57, v254, 61
	s_nop 3
	v_add_u32_e32 v138, s57, v196
	v_lshrrev_b32_e32 v139, 14, v138
	v_and_b32_e32 v143, 0x7f, v138
	v_lshl_or_b32 v139, v139, 7, v143
	v_lshlrev_b32_e32 v139, 2, v139
	v_lshlrev_b32_e32 v143, 1, v138
	v_lshlrev_b32_e32 v138, 2, v138
	v_mov_b32_e32 v134, 0
	s_add_u32 s84, s0, 0x33b5e000
	s_addc_u32 s85, s1, 0
	s_add_u32 s90, s0, 0x37d5e000
	s_addc_u32 s91, s1, 0
	s_add_u32 s98, s0, 0x31a14000
	s_addc_u32 s99, s1, 0
	s_mov_b32 s55, 0
	global_load_dword v135, v138, s[84:85] nt
	global_load_dword v136, v139, s[90:91]
.Lch_noinit:
.LBB0_425:
	ds_read_b128 v[64:67], v209 offset:49152
	ds_read_b128 v[68:71], v209 offset:57344
	ds_read_b128 v[190:193], v221 offset:49152
	ds_read_b128 v[228:231], v221 offset:57344
	v_add_f32_e32 v162, 0, v163
	v_add_f32_e32 v162, v177, v162
	s_waitcnt lgkmcnt(3)
	v_mfma_f32_32x32x16_bf16 v[80:95], v[64:67], v[118:121], 0
	v_add_f32_e32 v162, v164, v162
	v_add_f32_e32 v162, v188, v162
	v_add_f32_e32 v162, v176, v162
	v_add_f32_e32 v162, v189, v162
	v_add_f32_e32 v162, v165, v162
	v_add_f32_e32 v162, v175, v162
	v_add_f32_e32 v162, v166, v162
	s_waitcnt lgkmcnt(2)
	v_mfma_f32_32x32x16_bf16 v[64:79], v[68:71], v[118:121], 0
	v_add_f32_e32 v162, v173, v162
	v_add_f32_e32 v162, v167, v162
	v_add_f32_e32 v162, v174, v162
	v_exp_f32_e32 v160, v160
	v_add_f32_e32 v162, v168, v162
	v_exp_f32_e32 v161, v161
	v_add_f32_e32 v162, v171, v162
	s_waitcnt lgkmcnt(1)
	v_mfma_f32_32x32x16_bf16 v[80:95], v[190:193], v[126:129], v[80:95]
	s_cmp_eq_u32 s54, 0
	s_cbranch_scc1 .Lmv_f
	s_add_i32 m0, s52, 0x0
	s_nop 0
	global_load_lds_dwordx4 v130, s[48:49]
	s_add_i32 m0, s52, 0x400
	s_nop 0
	global_load_lds_dwordx4 v131, s[48:49]
	s_add_u32 s48, s48, 0x18000
	s_addc_u32 s49, s49, 0
	s_add_i32 m0, s53, 0x4000
	s_nop 0
	global_load_lds_dwordx4 v132, s[50:51]
	s_add_i32 m0, s53, 0x4400
	s_nop 0
	global_load_lds_dwordx4 v133, s[50:51]
	s_add_u32 s50, s50, 0xc0000
	s_addc_u32 s51, s51, 0
; #define SBAR() __builtin_amdgcn_sched_barrier(0)
; __device__ __forceinline__ void finishSM(f32x16& p0, f32x16& p1, float alpha, float& l_reg, bf16x8& pa0, bf16x8& pa1, bf16x8& pa2, bf16x8& pa3) {
;   for (int r = 0; r < 16; ++r) p1[r] = __builtin_amdgcn_exp2f(p1[r]);
;   float ps = 0; for (int r = 0; r < 16; ++r) ps += p0[r]; for (int r = 0; r < 16; ++r) ps += p1[r];
;   { auto rr = __builtin_amdgcn_permlane32_swap(__float_as_uint(ps), __float_as_uint(ps), false, false);
;     ps = __uint_as_float(rr[0]) + __uint_as_float(rr[1]); }
;   l_reg = l_reg * alpha + ps;
;     ...
;   PK4(p0, 0, pa0); PK4(p0, 8, pa1); PK4(p1, 0, pa2); PK4(p1, 8, pa3);
;     ...
; }
; template <bool HALF> __device__ __forceinline__ void qkt(f32x16& p0, f32x16& p1, const char* Ks, const bf16x8* qr, int r32, int hi, int koff) {
;   p0 = f32x16{}; p1 = f32x16{};
;   for (int d0 = 0; d0 < (HALF ? 4 : 8); ++d0) { int cb = (d0 * 16 + hi * 8) * 2 + koff;
;     bf16x8 b0 = *reinterpret_cast<const bf16x8*>(Ks + KSWZ(r32, cb));
;     bf16x8 b1 = *reinterpret_cast<const bf16x8*>(Ks + KSWZ(32 + r32, cb));
;     p0 = __builtin_amdgcn_mfma_f32_32x32x16_bf16(b0, qr[d0], p0, 0, 0, 0);
;     p1 = __builtin_amdgcn_mfma_f32_32x32x16_bf16(b1, qr[d0], p1, 0, 0, 0); }
; }
; __device__ __forceinline__ int v_st(int k, int c) { const int kk = (k & ~0xC) | ((k & 4) << 1) | ((k & 8) >> 1); return ((kk >> 3) * 4 + (c >> 5)) * 512 + ((kk & 7) * 32 + (c & 31)) * 2; }
; __device__ __forceinline__ int v_rd_base(int lane) { return ((lane & 3) << 3) | (((lane >> 2) & 3) << 6) | (((lane >> 4) & 1) << 5) | (((lane >> 5) & 1) << 8); }
; template <int OFF> __device__ __forceinline__ s16x4 tr_read(int vb) {
;   s16x4 r; asm volatile("ds_read_b64_tr_b16 %0, %1 offset:%2" : "=&v"(r) : "v"(vb), "i"(OFF) : "memory"); return r;
; }
; template <int D0> __device__ __forceinline__ void pv_one(f32x16& od, int vb, bf16x8 pa0, bf16x8 pa1, bf16x8 pa2, bf16x8 pa3) {
;   const s16x4 l0 = tr_read<v_rd_off(D0, 0, 0)>(vb), h0 = tr_read<v_rd_off(D0, 0, 1)>(vb), l1 = tr_read<v_rd_off(D0, 1, 0)>(vb), h1 = tr_read<v_rd_off(D0, 1, 1)>(vb);
;   const s16x4 l2 = tr_read<v_rd_off(D0, 2, 0)>(vb), h2 = tr_read<v_rd_off(D0, 2, 1)>(vb), l3 = tr_read<v_rd_off(D0, 3, 0)>(vb), h3 = tr_read<v_rd_off(D0, 3, 1)>(vb);
;   asm volatile("s_waitcnt lgkmcnt(0)" ::: "memory"); SBAR();
;     ...
;   od = __builtin_amdgcn_mfma_f32_32x32x16_bf16(pa0, PK(l0, h0), od, 0, 0, 0);
.Lmv_f:
	v_exp_f32_e32 v158, v158
	v_add_f32_e32 v162, v169, v162
	v_exp_f32_e32 v159, v159
	v_add_f32_e32 v162, v172, v162
	v_exp_f32_e32 v154, v154
	v_add_f32_e32 v162, v160, v162
	v_exp_f32_e32 v155, v155
	s_waitcnt lgkmcnt(0)
	v_mfma_f32_32x32x16_bf16 v[64:79], v[228:231], v[126:129], v[64:79]
	ds_read_b128 v[190:193], v222 offset:49152
	ds_read_b128 v[228:231], v222 offset:57344
	v_add_f32_e32 v162, v161, v162
	v_exp_f32_e32 v150, v150
	v_add_f32_e32 v162, v158, v162
	v_exp_f32_e32 v151, v151
	v_add_f32_e32 v162, v159, v162
	v_exp_f32_e32 v148, v148
	s_waitcnt lgkmcnt(1)
	v_mfma_f32_32x32x16_bf16 v[80:95], v[190:193], v[122:125], v[80:95]
	v_add_f32_e32 v162, v154, v162
	v_exp_f32_e32 v149, v149
	v_add_f32_e32 v162, v155, v162
	v_exp_f32_e32 v156, v156
	v_add_f32_e32 v162, v150, v162
	v_exp_f32_e32 v157, v157
	v_add_f32_e32 v162, v151, v162
	s_waitcnt lgkmcnt(0)
	v_mfma_f32_32x32x16_bf16 v[64:79], v[228:231], v[122:125], v[64:79]
	ds_read_b128 v[190:193], v210 offset:49152
	ds_read_b128 v[228:231], v210 offset:57344
	v_exp_f32_e32 v152, v152
	v_add_f32_e32 v162, v148, v162
	v_exp_f32_e32 v153, v153
	v_add_f32_e32 v162, v149, v162
	v_exp_f32_e32 v146, v146
	v_add_f32_e32 v162, v156, v162
	s_waitcnt lgkmcnt(1)
	v_mfma_f32_32x32x16_bf16 v[80:95], v[190:193], v[114:117], v[80:95]
	v_exp_f32_e32 v147, v147
	v_add_f32_e32 v162, v157, v162
	v_add_f32_e32 v162, v152, v162
	v_add_f32_e32 v162, v153, v162
	v_add_f32_e32 v162, v146, v162
	v_add_f32_e32 v227, v147, v162
	s_waitcnt lgkmcnt(0)
	v_mfma_f32_32x32x16_bf16 v[64:79], v[228:231], v[114:117], v[64:79]
	ds_read_b128 v[190:193], v211 offset:49152
	ds_read_b128 v[228:231], v211 offset:57344
	s_waitcnt lgkmcnt(1)
	v_mfma_f32_32x32x16_bf16 v[80:95], v[190:193], v[110:113], v[80:95]
	s_waitcnt lgkmcnt(0)
	v_mfma_f32_32x32x16_bf16 v[64:79], v[228:231], v[110:113], v[64:79]
	ds_read_b128 v[190:193], v223 offset:49152
	ds_read_b128 v[228:231], v223 offset:57344
	s_waitcnt lgkmcnt(1)
	v_mfma_f32_32x32x16_bf16 v[80:95], v[190:193], v[106:109], v[80:95]
	s_waitcnt lgkmcnt(0)
	v_mfma_f32_32x32x16_bf16 v[64:79], v[228:231], v[106:109], v[64:79]
	ds_read_b128 v[190:193], v225 offset:49152
	ds_read_b128 v[228:231], v225 offset:57344
	s_waitcnt lgkmcnt(1)
	v_mfma_f32_32x32x16_bf16 v[80:95], v[190:193], v[102:105], v[80:95]
	s_waitcnt lgkmcnt(0)
	v_mfma_f32_32x32x16_bf16 v[64:79], v[228:231], v[102:105], v[64:79]
	ds_read_b128 v[190:193], v224 offset:49152
	ds_read_b128 v[228:231], v224 offset:57344
	v_cvt_pk_bf16_f32 v162, v163, v177
	v_cvt_pk_bf16_f32 v163, v164, v188
	v_cvt_pk_bf16_f32 v164, v176, v189
	v_cvt_pk_bf16_f32 v165, v165, v175
	v_cvt_pk_bf16_f32 v166, v166, v173
	v_cvt_pk_bf16_f32 v167, v167, v174
	s_waitcnt lgkmcnt(1)
	v_mfma_f32_32x32x16_bf16 v[80:95], v[190:193], v[98:101], v[80:95]
	v_permlane32_swap_b32_e32 v162, v164
	v_cvt_pk_bf16_f32 v168, v168, v171
	v_cvt_pk_bf16_f32 v169, v169, v172
	v_cvt_pk_bf16_f32 v172, v160, v161
	v_cvt_pk_bf16_f32 v173, v158, v159
	v_cvt_pk_bf16_f32 v174, v154, v155
	s_waitcnt lgkmcnt(0)
	v_mfma_f32_32x32x16_bf16 v[64:79], v[228:231], v[98:101], v[64:79]
	v_mov_b32_e32 v228, v227
	s_nop 1
	v_permlane32_swap_b32_e32 v227, v228
	v_cvt_pk_bf16_f32 v175, v150, v151
	v_cvt_pk_bf16_f32 v230, v148, v149
	v_cvt_pk_bf16_f32 v231, v156, v157
	v_cvt_pk_bf16_f32 v232, v152, v153
	v_cvt_pk_bf16_f32 v233, v146, v147
	v_permlane32_swap_b32_e32 v163, v165
	v_permlane32_swap_b32_e32 v166, v168
	v_permlane32_swap_b32_e32 v167, v169
	v_permlane32_swap_b32_e32 v172, v174
	v_permlane32_swap_b32_e32 v173, v175
	v_permlane32_swap_b32_e32 v230, v232
	v_permlane32_swap_b32_e32 v231, v233
	ds_read_b64_tr_b16 v[234:235], v204 offset:0
	ds_read_b64_tr_b16 v[236:237], v204 offset:0x800
	ds_read_b64_tr_b16 v[238:239], v204 offset:0x1000
	ds_read_b64_tr_b16 v[240:241], v204 offset:0x1800
	ds_read_b64_tr_b16 v[242:243], v204 offset:0x2000
	ds_read_b64_tr_b16 v[244:245], v204 offset:0x2800
	ds_read_b64_tr_b16 v[246:247], v204 offset:0x3000
	ds_read_b64_tr_b16 v[248:249], v204 offset:0x3800
	s_waitcnt lgkmcnt(0)
	s_nop 0
	v_mfma_f32_32x32x16_bf16 v[0:15], v[162:165], v[234:237], v[0:15]
	ds_read_b64_tr_b16 v[234:235], v204 offset:0x200
	ds_read_b64_tr_b16 v[236:237], v204 offset:0xa00
	v_mfma_f32_32x32x16_bf16 v[0:15], v[166:169], v[238:241], v[0:15]
	ds_read_b64_tr_b16 v[238:239], v204 offset:0x1200
	ds_read_b64_tr_b16 v[240:241], v204 offset:0x1a00
	v_mfma_f32_32x32x16_bf16 v[0:15], v[172:175], v[242:245], v[0:15]
	ds_read_b64_tr_b16 v[242:243], v204 offset:0x2200
	ds_read_b64_tr_b16 v[244:245], v204 offset:0x2a00
	v_mfma_f32_32x32x16_bf16 v[0:15], v[230:233], v[246:249], v[0:15]
	ds_read_b64_tr_b16 v[246:247], v204 offset:0x3200
	ds_read_b64_tr_b16 v[248:249], v204 offset:0x3a00
	s_waitcnt lgkmcnt(0)
; #define SBAR() __builtin_amdgcn_sched_barrier(0)
; #define SWRITE(b, i) do { *(LAS bf16x8*)(V_lds + (b) * SHM_V + vst0) = sr_[i].vs0;          \
;     *(LAS bf16x8*)(V_lds + (b) * SHM_V + vst1) = sr_[i].vs1; int kc = sc * 2;               \
;     *(LAS bf16x8*)(K_lds + (b) * SHM_K + KSWZ(sr, kc)) = sr_[i].ks0;                       \
;     *(LAS bf16x8*)(K_lds + (b) * SHM_K + KSWZ(32 + sr, kc)) = sr_[i].ks1; } while (0)
; #define SWAIT() asm volatile("s_waitcnt vmcnt(4)" ::: "memory")
; #define H2_STEP(V, D, C0) do { _Pragma("unroll") for (int u = 0; u < 6; ++u) { sb[(size_t)((C0) + u) * 8 * 16384] = f2bf(S); S = fmaf(D[u], S, V[u]); } } while (0)
; template <bool HALF> __device__ __forceinline__ void dense_body(const bf16_t* __restrict__ Qb, const bf16_t* __restrict__ Kh, const bf16_t* __restrict__ Vh, ...
;     ...
;   f32x16 pA0, pA1, pB0, pB1; float mnA, mnB, alA, alB; bf16x8 pa0, pa1, pa2, pa3; const int NT = seq / KVBLK;
;   const char* Kl0 = (const char*)K_lds; const char* Kl1 = (const char*)(K_lds + SHM_K);
;   constexpr int SE = 0, SO = 1;
;   SLOAD(SE, 0); asm volatile("s_waitcnt vmcnt(0)" ::: "memory"); SWRITE(0, SE); __syncthreads();
;   qkt<HALF>(pA0, pA1, Kl0, qr, r32, hi, koff); partialSM(pA0, pA1, m_reg, mnA, alA);
;   SLOAD(SO, KVBLK); if (2 < NT) SLOAD(SE, 2 * KVBLK);
;   SWAIT(); SWRITE(1, SO); __syncthreads();
;   for (int j = 1; j + 1 < NT; j += 2) {
;     SBAR(); qkt<HALF>(pB0, pB1, Kl1, qr, r32, hi, koff);
;     finishSM(pA0, pA1, alA, l_reg, pa0, pa1, pa2, pa3); SBAR();
;     SLOAD(SO, (j + 2) * KVBLK); SBAR();
;     pv_d0(o, vb0, pa0, pa1, pa2, pa3); partialSM(pB0, pB1, m_reg, mnB, alB);
;     __syncthreads(); SWAIT(); SWRITE(0, SE);
;     RESC(alB); __syncthreads();
; __device__ __forceinline__ void ph_hgrn_chain2(const P& p, int gt, int nt) {
;   for (int idx = gt; idx < 8 * 128 * 128; idx += nt) {
;     const int hd = idx >> 14, ed = idx & 16383, d = ed & 127;
;     const float* kv = WSP(float, WS_KVC) + (size_t)hd * 16384 + ed; const float* dc = WSP(float, WS_DEC) + hd * 128 + d; bf16_t* sb = WSP(bf16_t, WS_SB) + (size_t)hd * 16384 + ed;
;     float S = 0.f;
;     float a[6], da[6], b2[6], db[6];
;     ...
;     H2_LOAD(a, da, 0);
; #pragma unroll 1
;     for (int c0 = 0; c0 < HG_NCH; c0 += 12) {
;       H2_LOAD(b2, db, c0 + 6); H2_STEP(a, da, c0);
;       if (c0 + 12 < HG_NCH) H2_LOAD(a, da, c0 + 12);
;       H2_STEP(b2, db, c0 + 6);
;     }
	v_mfma_f32_32x32x16_bf16 v[48:63], v[162:165], v[234:237], v[48:63]
	ds_read_b64_tr_b16 v[234:235], v204 offset:0x400
	ds_read_b64_tr_b16 v[236:237], v204 offset:0xc00
	v_mfma_f32_32x32x16_bf16 v[48:63], v[166:169], v[238:241], v[48:63]
	ds_read_b64_tr_b16 v[238:239], v204 offset:0x1400
	ds_read_b64_tr_b16 v[240:241], v204 offset:0x1c00
	v_mfma_f32_32x32x16_bf16 v[48:63], v[172:175], v[242:245], v[48:63]
	ds_read_b64_tr_b16 v[242:243], v204 offset:0x2400
	ds_read_b64_tr_b16 v[244:245], v204 offset:0x2c00
	v_mfma_f32_32x32x16_bf16 v[48:63], v[230:233], v[246:249], v[48:63]
	ds_read_b64_tr_b16 v[246:247], v204 offset:0x3400
	ds_read_b64_tr_b16 v[248:249], v204 offset:0x3c00
	s_waitcnt lgkmcnt(0)
	v_mfma_f32_32x32x16_bf16 v[32:47], v[162:165], v[234:237], v[32:47]
	ds_read_b64_tr_b16 v[234:235], v204 offset:0x600
	ds_read_b64_tr_b16 v[236:237], v204 offset:0xe00
	v_mfma_f32_32x32x16_bf16 v[32:47], v[166:169], v[238:241], v[32:47]
	ds_read_b64_tr_b16 v[238:239], v204 offset:0x1600
	ds_read_b64_tr_b16 v[240:241], v204 offset:0x1e00
	v_mfma_f32_32x32x16_bf16 v[32:47], v[172:175], v[242:245], v[32:47]
	ds_read_b64_tr_b16 v[242:243], v204 offset:0x2600
	ds_read_b64_tr_b16 v[244:245], v204 offset:0x2e00
	v_mfma_f32_32x32x16_bf16 v[32:47], v[230:233], v[246:249], v[32:47]
	ds_read_b64_tr_b16 v[246:247], v204 offset:0x3600
	ds_read_b64_tr_b16 v[248:249], v204 offset:0x3e00
	s_waitcnt lgkmcnt(0)
	v_mfma_f32_32x32x16_bf16 v[16:31], v[162:165], v[234:237], v[16:31]
	v_max_f32_e32 v162, v81, v81
	v_max_f32_e32 v163, v80, v80
	v_max_f32_e32 v162, v163, v162
	v_max3_f32 v162, v162, v82, v83
	v_max3_f32 v162, v162, v84, v85
	v_max3_f32 v162, v162, v86, v87
	v_max3_f32 v162, v162, v88, v89
	v_max3_f32 v162, v162, v90, v91
	v_max3_f32 v162, v162, v92, v93
	v_mfma_f32_32x32x16_bf16 v[16:31], v[166:169], v[238:241], v[16:31]
	v_max3_f32 v162, v162, v94, v95
	v_max3_f32 v162, v162, v64, v65
	v_max3_f32 v162, v162, v66, v67
	v_max3_f32 v162, v162, v68, v69
	v_max3_f32 v162, v162, v70, v71
	v_max3_f32 v162, v162, v72, v73
	v_max3_f32 v162, v162, v74, v75
	v_max3_f32 v162, v162, v76, v77
	v_mfma_f32_32x32x16_bf16 v[16:31], v[172:175], v[242:245], v[16:31]
	v_max3_f32 v162, v162, v78, v79
	v_mov_b32_e32 v163, v162
	s_nop 1
	v_permlane32_swap_b32_e32 v162, v163
	v_max_f32_e32 v163, v163, v163
	v_max_f32_e32 v162, v162, v162
	v_max_f32_e32 v162, v162, v163
	v_sub_f32_e32 v163, v162, v170
	v_cmp_ge_f32_e32 vcc, s87, v163
	v_max_f32_e32 v163, v170, v170
	v_max_f32_e32 v162, v163, v162
	v_mfma_f32_32x32x16_bf16 v[16:31], v[230:233], v[246:249], v[16:31]
	v_sub_f32_e32 v163, v170, v162
	v_mul_f32_e32 v163, 0x3e0293ee, v163
	v_exp_f32_e32 v163, v163
	s_cmp_eq_u64 vcc, exec
	s_cselect_b64 s[42:43], -1, 0
	s_waitcnt vmcnt(0)
	s_barrier
	s_cmp_ge_u32 s55, 0x84
	s_cbranch_scc1 .Lch_sa
	v_bfe_u32 v137, v134, 16, 1
	v_add3_u32 v137, v134, v137, s86
	global_store_short_d16_hi v143, v137, s[98:99]
	v_fma_f32 v134, v136, v134, v135
	v_add_u32_e32 v138, 0x80000, v138
	v_add_u32_e32 v139, 0x1000, v139
	v_add_u32_e32 v143, 0x40000, v143
	s_add_i32 s55, s55, 1
	global_load_dword v135, v138, s[84:85] nt
	global_load_dword v136, v139, s[90:91]
.Lch_sa:
	v_cndmask_b32_e64 v229, v163, 1.0, s[42:43]
	v_cmp_gt_f32_e32 vcc, 1.0, v229
	s_cbranch_vccz .LBB0_429
	s_and_saveexec_b64 s[6:7], s[40:41]
	ds_write_b32 v201, v229 offset:128
	s_or_b64 exec, exec, s[6:7]
	s_waitcnt lgkmcnt(0)
	v_add_u32_e32 v163, v200, v96
	ds_read_b128 v[164:167], v163 offset:224
	ds_read_b128 v[172:175], v163 offset:192
	ds_read_b128 v[230:233], v163 offset:160
	ds_read_b128 v[234:237], v163 offset:128
	s_waitcnt lgkmcnt(3)
	v_pk_mul_f32 v[12:13], v[12:13], v[164:165]
	s_waitcnt lgkmcnt(2)
	v_pk_mul_f32 v[8:9], v[8:9], v[172:173]
	s_waitcnt lgkmcnt(1)
	v_pk_mul_f32 v[4:5], v[4:5], v[230:231]
	v_pk_mul_f32 v[14:15], v[14:15], v[166:167]
	v_pk_mul_f32 v[10:11], v[10:11], v[174:175]
	v_pk_mul_f32 v[6:7], v[6:7], v[232:233]
	s_waitcnt lgkmcnt(0)
	v_pk_mul_f32 v[2:3], v[2:3], v[236:237]
	v_pk_mul_f32 v[0:1], v[0:1], v[234:235]
	v_pk_mul_f32 v[60:61], v[60:61], v[164:165]
	v_pk_mul_f32 v[56:57], v[56:57], v[172:173]
	v_pk_mul_f32 v[52:53], v[52:53], v[230:231]
	v_pk_mul_f32 v[62:63], v[62:63], v[166:167]
	v_pk_mul_f32 v[58:59], v[58:59], v[174:175]
	v_pk_mul_f32 v[54:55], v[54:55], v[232:233]
	v_pk_mul_f32 v[50:51], v[50:51], v[236:237]
	v_pk_mul_f32 v[48:49], v[48:49], v[234:235]
	v_pk_mul_f32 v[44:45], v[44:45], v[164:165]
	v_pk_mul_f32 v[40:41], v[40:41], v[172:173]
	v_pk_mul_f32 v[36:37], v[36:37], v[230:231]
	v_pk_mul_f32 v[46:47], v[46:47], v[166:167]
	v_pk_mul_f32 v[42:43], v[42:43], v[174:175]
	v_pk_mul_f32 v[38:39], v[38:39], v[232:233]
	v_pk_mul_f32 v[34:35], v[34:35], v[236:237]
	v_pk_mul_f32 v[32:33], v[32:33], v[234:235]
	v_pk_mul_f32 v[28:29], v[28:29], v[164:165]
	v_pk_mul_f32 v[24:25], v[24:25], v[172:173]
	v_pk_mul_f32 v[20:21], v[20:21], v[230:231]
	v_pk_mul_f32 v[30:31], v[30:31], v[166:167]
	v_pk_mul_f32 v[26:27], v[26:27], v[174:175]
	v_pk_mul_f32 v[22:23], v[22:23], v[232:233]
	v_pk_mul_f32 v[18:19], v[18:19], v[236:237]
	v_pk_mul_f32 v[16:17], v[16:17], v[234:235]

; #define SBAR() __builtin_amdgcn_sched_barrier(0)
; #define SWRITE(b, i) do { *(LAS bf16x8*)(V_lds + (b) * SHM_V + vst0) = sr_[i].vs0;          \
;     *(LAS bf16x8*)(V_lds + (b) * SHM_V + vst1) = sr_[i].vs1; int kc = sc * 2;               \
;     *(LAS bf16x8*)(K_lds + (b) * SHM_K + KSWZ(sr, kc)) = sr_[i].ks0;                       \
;     *(LAS bf16x8*)(K_lds + (b) * SHM_K + KSWZ(32 + sr, kc)) = sr_[i].ks1; } while (0)
; #define SWAIT() asm volatile("s_waitcnt vmcnt(4)" ::: "memory")
; #define H2_STEP(V, D, C0) do { _Pragma("unroll") for (int u = 0; u < 6; ++u) { sb[(size_t)((C0) + u) * 8 * 16384] = f2bf(S); S = fmaf(D[u], S, V[u]); } } while (0)
; template <bool HALF> __device__ __forceinline__ void dense_body(const bf16_t* __restrict__ Qb, const bf16_t* __restrict__ Kh, const bf16_t* __restrict__ Vh, ...
;     ...
;   f32x16 pA0, pA1, pB0, pB1; float mnA, mnB, alA, alB; bf16x8 pa0, pa1, pa2, pa3; const int NT = seq / KVBLK;
;   const char* Kl0 = (const char*)K_lds; const char* Kl1 = (const char*)(K_lds + SHM_K);
;   constexpr int SE = 0, SO = 1;
;   SLOAD(SE, 0); asm volatile("s_waitcnt vmcnt(0)" ::: "memory"); SWRITE(0, SE); __syncthreads();
;   qkt<HALF>(pA0, pA1, Kl0, qr, r32, hi, koff); partialSM(pA0, pA1, m_reg, mnA, alA);
;   SLOAD(SO, KVBLK); if (2 < NT) SLOAD(SE, 2 * KVBLK);
;   SWAIT(); SWRITE(1, SO); __syncthreads();
;   for (int j = 1; j + 1 < NT; j += 2) {
;     SBAR(); qkt<HALF>(pB0, pB1, Kl1, qr, r32, hi, koff);
;     finishSM(pA0, pA1, alA, l_reg, pa0, pa1, pa2, pa3); SBAR();
;     SLOAD(SO, (j + 2) * KVBLK); SBAR();
;     pv_d0(o, vb0, pa0, pa1, pa2, pa3); partialSM(pB0, pB1, m_reg, mnB, alB);
;     __syncthreads(); SWAIT(); SWRITE(0, SE);
;     RESC(alB); __syncthreads();
; __device__ __forceinline__ void ph_hgrn_chain2(const P& p, int gt, int nt) {
;   for (int idx = gt; idx < 8 * 128 * 128; idx += nt) {
;     const int hd = idx >> 14, ed = idx & 16383, d = ed & 127;
;     const float* kv = WSP(float, WS_KVC) + (size_t)hd * 16384 + ed; const float* dc = WSP(float, WS_DEC) + hd * 128 + d; bf16_t* sb = WSP(bf16_t, WS_SB) + (size_t)hd * 16384 + ed;
;     float S = 0.f;
;     float a[6], da[6], b2[6], db[6];
;     ...
;     H2_LOAD(a, da, 0);
; #pragma unroll 1
;     for (int c0 = 0; c0 < HG_NCH; c0 += 12) {
;       H2_LOAD(b2, db, c0 + 6); H2_STEP(a, da, c0);
;       if (c0 + 12 < HG_NCH) H2_LOAD(a, da, c0 + 12);
;       H2_STEP(b2, db, c0 + 6);
;     }
.LBB0_431:
	ds_read_b64_tr_b16 v[188:189], v203 offset:0
	ds_read_b64_tr_b16 v[190:191], v203 offset:0x800
	ds_read_b64_tr_b16 v[192:193], v203 offset:0x1000
	ds_read_b64_tr_b16 v[194:195], v203 offset:0x1800
	ds_read_b64_tr_b16 v[212:213], v203 offset:0x2000
	ds_read_b64_tr_b16 v[214:215], v203 offset:0x2800
	ds_read_b64_tr_b16 v[234:235], v203 offset:0x3000
	ds_read_b64_tr_b16 v[236:237], v203 offset:0x3800
	s_waitcnt lgkmcnt(0)
	s_nop 0
	v_mfma_f32_32x32x16_bf16 v[0:15], v[162:165], v[188:191], v[0:15]
	ds_read_b64_tr_b16 v[188:189], v203 offset:0x200
	ds_read_b64_tr_b16 v[190:191], v203 offset:0xa00
	v_mfma_f32_32x32x16_bf16 v[0:15], v[166:169], v[192:195], v[0:15]
	ds_read_b64_tr_b16 v[192:193], v203 offset:0x1200
	ds_read_b64_tr_b16 v[194:195], v203 offset:0x1a00
	v_mfma_f32_32x32x16_bf16 v[0:15], v[170:173], v[212:215], v[0:15]
	ds_read_b64_tr_b16 v[212:213], v203 offset:0x2200
	ds_read_b64_tr_b16 v[214:215], v203 offset:0x2a00
	v_mfma_f32_32x32x16_bf16 v[0:15], v[174:177], v[234:237], v[0:15]
	ds_read_b64_tr_b16 v[234:235], v203 offset:0x3200
	ds_read_b64_tr_b16 v[236:237], v203 offset:0x3a00
	s_waitcnt lgkmcnt(0)
	v_mfma_f32_32x32x16_bf16 v[48:63], v[162:165], v[188:191], v[48:63]
	ds_read_b64_tr_b16 v[188:189], v203 offset:0x400
	ds_read_b64_tr_b16 v[190:191], v203 offset:0xc00
	v_mfma_f32_32x32x16_bf16 v[48:63], v[166:169], v[192:195], v[48:63]
	ds_read_b64_tr_b16 v[192:193], v203 offset:0x1400
	ds_read_b64_tr_b16 v[194:195], v203 offset:0x1c00
	v_mfma_f32_32x32x16_bf16 v[48:63], v[170:173], v[212:215], v[48:63]
	ds_read_b64_tr_b16 v[212:213], v203 offset:0x2400
	ds_read_b64_tr_b16 v[214:215], v203 offset:0x2c00
	v_mfma_f32_32x32x16_bf16 v[48:63], v[174:177], v[234:237], v[48:63]
	ds_read_b64_tr_b16 v[234:235], v203 offset:0x3400
	ds_read_b64_tr_b16 v[236:237], v203 offset:0x3c00
	s_waitcnt lgkmcnt(0)
	v_mfma_f32_32x32x16_bf16 v[32:47], v[162:165], v[188:191], v[32:47]
	ds_read_b64_tr_b16 v[188:189], v203 offset:0x600
	ds_read_b64_tr_b16 v[190:191], v203 offset:0xe00
	v_mfma_f32_32x32x16_bf16 v[32:47], v[166:169], v[192:195], v[32:47]
	ds_read_b64_tr_b16 v[192:193], v203 offset:0x1600
	ds_read_b64_tr_b16 v[194:195], v203 offset:0x1e00
	v_mfma_f32_32x32x16_bf16 v[32:47], v[170:173], v[212:215], v[32:47]
	ds_read_b64_tr_b16 v[212:213], v203 offset:0x2600
	ds_read_b64_tr_b16 v[214:215], v203 offset:0x2e00
	v_mfma_f32_32x32x16_bf16 v[32:47], v[174:177], v[234:237], v[32:47]
	ds_read_b64_tr_b16 v[234:235], v203 offset:0x3600
	ds_read_b64_tr_b16 v[236:237], v203 offset:0x3e00
	s_waitcnt lgkmcnt(0)
	v_mfma_f32_32x32x16_bf16 v[16:31], v[162:165], v[188:191], v[16:31]
	v_max_f32_e32 v162, v81, v81
	v_max_f32_e32 v163, v80, v80
	v_max_f32_e32 v162, v163, v162
	v_max3_f32 v162, v162, v82, v83
	v_max3_f32 v162, v162, v84, v85
	v_max3_f32 v162, v162, v86, v87
	v_max3_f32 v162, v162, v88, v89
	v_max3_f32 v162, v162, v90, v91
	v_max3_f32 v162, v162, v92, v93
	v_mfma_f32_32x32x16_bf16 v[16:31], v[166:169], v[192:195], v[16:31]
	v_max3_f32 v162, v162, v94, v95
	v_max3_f32 v162, v162, v64, v65
	v_max3_f32 v162, v162, v66, v67
	v_max3_f32 v162, v162, v68, v69
	v_max3_f32 v162, v162, v70, v71
	v_max3_f32 v162, v162, v72, v73
	v_max3_f32 v162, v162, v74, v75
	v_max3_f32 v162, v162, v76, v77
	v_mfma_f32_32x32x16_bf16 v[16:31], v[170:173], v[212:215], v[16:31]
	v_max3_f32 v162, v162, v78, v79
	v_mov_b32_e32 v163, v162
	s_nop 1
	v_permlane32_swap_b32_e32 v162, v163
	v_max_f32_e32 v163, v163, v163
	v_max_f32_e32 v162, v162, v162
	v_max_f32_e32 v162, v162, v163
	v_sub_f32_e32 v163, v162, v230
	v_cmp_ge_f32_e32 vcc, s87, v163
	v_max_f32_e32 v163, v230, v230
	v_max_f32_e32 v163, v163, v162
	v_mfma_f32_32x32x16_bf16 v[16:31], v[174:177], v[234:237], v[16:31]
	v_sub_f32_e32 v162, v230, v163
	v_mul_f32_e32 v162, 0x3e0293ee, v162
	v_exp_f32_e32 v162, v162
	s_cmp_eq_u64 vcc, exec
	s_cselect_b64 s[42:43], -1, 0
	s_waitcnt vmcnt(0)
	s_barrier
	s_cmp_ge_u32 s55, 0x84
	s_cbranch_scc1 .Lch_sb
	v_bfe_u32 v137, v134, 16, 1
	v_add3_u32 v137, v134, v137, s86
	global_store_short_d16_hi v143, v137, s[98:99]
	v_fma_f32 v134, v136, v134, v135
	v_add_u32_e32 v138, 0x80000, v138
	v_add_u32_e32 v139, 0x1000, v139
	v_add_u32_e32 v143, 0x40000, v143
	s_add_i32 s55, s55, 1
	global_load_dword v135, v138, s[84:85] nt
	global_load_dword v136, v139, s[90:91]
.Lch_sb:
	s_mov_b32 s54, 1
	v_cndmask_b32_e64 v162, v162, 1.0, s[42:43]
	v_cmp_gt_f32_e32 vcc, 1.0, v162
	s_cbranch_vccz .LBB0_435
	s_and_saveexec_b64 s[6:7], s[40:41]
	ds_write_b32 v201, v162 offset:128
	s_or_b64 exec, exec, s[6:7]
	s_waitcnt lgkmcnt(0)
	v_add_u32_e32 v158, v200, v96
	ds_read_b128 v[146:149], v158 offset:224
	ds_read_b128 v[150:153], v158 offset:192
	ds_read_b128 v[154:157], v158 offset:160
	ds_read_b128 v[158:161], v158 offset:128
	s_waitcnt lgkmcnt(3)
	v_pk_mul_f32 v[12:13], v[12:13], v[146:147]
	s_waitcnt lgkmcnt(2)
	v_pk_mul_f32 v[8:9], v[8:9], v[150:151]
	s_waitcnt lgkmcnt(1)
	v_pk_mul_f32 v[4:5], v[4:5], v[154:155]
	v_pk_mul_f32 v[14:15], v[14:15], v[148:149]
	v_pk_mul_f32 v[10:11], v[10:11], v[152:153]
	v_pk_mul_f32 v[6:7], v[6:7], v[156:157]
	s_waitcnt lgkmcnt(0)
	v_pk_mul_f32 v[2:3], v[2:3], v[160:161]
	v_pk_mul_f32 v[0:1], v[0:1], v[158:159]
	v_pk_mul_f32 v[60:61], v[60:61], v[146:147]
	v_pk_mul_f32 v[56:57], v[56:57], v[150:151]
	v_pk_mul_f32 v[52:53], v[52:53], v[154:155]
	v_pk_mul_f32 v[62:63], v[62:63], v[148:149]
	v_pk_mul_f32 v[58:59], v[58:59], v[152:153]
	v_pk_mul_f32 v[54:55], v[54:55], v[156:157]
	v_pk_mul_f32 v[50:51], v[50:51], v[160:161]
	v_pk_mul_f32 v[48:49], v[48:49], v[158:159]
	v_pk_mul_f32 v[44:45], v[44:45], v[146:147]
	v_pk_mul_f32 v[40:41], v[40:41], v[150:151]
	v_pk_mul_f32 v[36:37], v[36:37], v[154:155]
	v_pk_mul_f32 v[46:47], v[46:47], v[148:149]
	v_pk_mul_f32 v[42:43], v[42:43], v[152:153]
	v_pk_mul_f32 v[38:39], v[38:39], v[156:157]
	v_pk_mul_f32 v[34:35], v[34:35], v[160:161]
	v_pk_mul_f32 v[32:33], v[32:33], v[158:159]
	v_pk_mul_f32 v[28:29], v[28:29], v[146:147]
	v_pk_mul_f32 v[24:25], v[24:25], v[150:151]
	v_pk_mul_f32 v[20:21], v[20:21], v[154:155]
	v_pk_mul_f32 v[30:31], v[30:31], v[148:149]
	v_pk_mul_f32 v[26:27], v[26:27], v[152:153]
	v_pk_mul_f32 v[22:23], v[22:23], v[156:157]
	v_pk_mul_f32 v[18:19], v[18:19], v[160:161]
	v_pk_mul_f32 v[16:17], v[16:17], v[158:159]

; #define H2_LOAD(V, D, C0) do { _Pragma("unroll") for (int u = 0; u < 6; ++u) { V[u] = __builtin_nontemporal_load(kv + (size_t)((C0) + u) * 8 * 16384); D[u] = dc[(size_t)((C0) + u) * 8 * 128]; } } while (0)
; #define H2_STEP(V, D, C0) do { _Pragma("unroll") for (int u = 0; u < 6; ++u) { sb[(size_t)((C0) + u) * 8 * 16384] = f2bf(S); S = fmaf(D[u], S, V[u]); } } while (0)
; __device__ __forceinline__ void ph_hgrn_chain2(const P& p, int gt, int nt) {
;   for (int idx = gt; idx < 8 * 128 * 128; idx += nt) {
;     const int hd = idx >> 14, ed = idx & 16383, d = ed & 127;
;     const float* kv = WSP(float, WS_KVC) + (size_t)hd * 16384 + ed; const float* dc = WSP(float, WS_DEC) + hd * 128 + d; bf16_t* sb = WSP(bf16_t, WS_SB) + (size_t)hd * 16384 + ed;
;     float S = 0.f;
;     float a[6], da[6], b2[6], db[6];
;     ...
;     H2_LOAD(a, da, 0);
; #pragma unroll 1
;     for (int c0 = 0; c0 < HG_NCH; c0 += 12) {
;       H2_LOAD(b2, db, c0 + 6); H2_STEP(a, da, c0);
;       if (c0 + 12 < HG_NCH) H2_LOAD(a, da, c0 + 12);
;       H2_STEP(b2, db, c0 + 6);
;     }
.LBB0_437:
.Lch_fin:
	s_cmp_ge_u32 s55, 0x84
	s_cbranch_scc1 .Lch_done
	s_waitcnt vmcnt(0)
	v_bfe_u32 v137, v134, 16, 1
	v_add3_u32 v137, v134, v137, s86
	global_store_short_d16_hi v143, v137, s[98:99]
	v_fma_f32 v134, v136, v134, v135
	v_add_u32_e32 v138, 0x80000, v138
	v_add_u32_e32 v139, 0x1000, v139
	v_add_u32_e32 v143, 0x40000, v143
	s_add_i32 s55, s55, 1
	global_load_dword v135, v138, s[84:85] nt
	global_load_dword v136, v139, s[90:91]
	s_branch .Lch_fin
